# top-n loop: lane-select mask built with s_ff1/s_lshl_b64 (drops one VALU compare and the two wait states per token-round)
# baseline (speedup 1.0000x reference)
; __device__ __forceinline__ void topn_round_u(unsigned (&k)[4], unsigned& pm, int lane) {
;     const unsigned wm = wave_max_u(k[0]);
;     const unsigned long long bal = __ballot(k[0] == wm); const int L = __ffsll((long long)bal) - 1;
;     const bool isL = lane == L;
;     pm |= isL ? (8u >> (k[0] & 3u)) : 0u;
;     k[0] = isL ? k[1] : k[0]; k[1] = isL ? k[2] : k[1]; k[2] = isL ? k[3] : k[2]; k[3] = isL ? 0u : k[3];
; }
; __device__ __forceinline__ void cmp_phase(Frame& F) {
;     ...
;                 for (int r = 0; r < TOPN - 3; ++r) { topn_round_u(ka, pa, lane); topn_round_u(kb2, pb, lane); topn_round_u(kc, pc, lane); topn_round_u(kd, pd, lane); }
;                 const unsigned bt = 1u << tk;
; #pragma unroll
;                 for (int q = 0; q < 4; ++q) pick[q] |= (((pa >> q) & 1u) ? bt : 0u) | (((pb >> q) & 1u) ? (bt << 1) : 0u) | (((pc >> q) & 1u) ? (bt << 2) : 0u) | (((pd >> q) & 1u) ? (bt << 3) : 0u);
.LBB0_1622:
	v_max_u32_dpp v24, v6, v6 quad_perm:[1,0,3,2] row_mask:0xf bank_mask:0xf bound_ctrl:1
	v_max_u32_dpp v26, v12, v12 quad_perm:[1,0,3,2] row_mask:0xf bank_mask:0xf bound_ctrl:1
	v_max_u32_dpp v28, v16, v16 quad_perm:[1,0,3,2] row_mask:0xf bank_mask:0xf bound_ctrl:1
	v_max_u32_dpp v30, v20, v20 quad_perm:[1,0,3,2] row_mask:0xf bank_mask:0xf bound_ctrl:1
	v_max_u32_dpp v24, v24, v24 quad_perm:[2,3,0,1] row_mask:0xf bank_mask:0xf bound_ctrl:1
	v_max_u32_dpp v26, v26, v26 quad_perm:[2,3,0,1] row_mask:0xf bank_mask:0xf bound_ctrl:1
	v_max_u32_dpp v28, v28, v28 quad_perm:[2,3,0,1] row_mask:0xf bank_mask:0xf bound_ctrl:1
	v_max_u32_dpp v30, v30, v30 quad_perm:[2,3,0,1] row_mask:0xf bank_mask:0xf bound_ctrl:1
	v_max_u32_dpp v24, v24, v24 row_half_mirror row_mask:0xf bank_mask:0xf bound_ctrl:1
	v_max_u32_dpp v26, v26, v26 row_half_mirror row_mask:0xf bank_mask:0xf bound_ctrl:1
	v_max_u32_dpp v28, v28, v28 row_half_mirror row_mask:0xf bank_mask:0xf bound_ctrl:1
	v_max_u32_dpp v30, v30, v30 row_half_mirror row_mask:0xf bank_mask:0xf bound_ctrl:1
	v_max_u32_dpp v24, v24, v24 row_mirror row_mask:0xf bank_mask:0xf bound_ctrl:1
	v_max_u32_dpp v26, v26, v26 row_mirror row_mask:0xf bank_mask:0xf bound_ctrl:1
	v_max_u32_dpp v28, v28, v28 row_mirror row_mask:0xf bank_mask:0xf bound_ctrl:1
	v_max_u32_dpp v30, v30, v30 row_mirror row_mask:0xf bank_mask:0xf bound_ctrl:1
	v_readlane_b32 s18, v24, 0
	v_readlane_b32 s19, v24, 16
	v_readlane_b32 s22, v24, 32
	v_readlane_b32 s23, v24, 48
	v_readlane_b32 s24, v26, 0
	v_readlane_b32 s25, v26, 16
	v_readlane_b32 s48, v26, 32
	v_readlane_b32 s74, v26, 48
	s_max_u32 s18, s18, s19
	s_max_u32 s22, s22, s23
	s_max_u32 s18, s18, s22
	s_max_u32 s24, s24, s25
	s_max_u32 s48, s48, s74
	s_max_u32 s24, s24, s48
	v_readlane_b32 s48, v28, 0
	v_readlane_b32 s19, v28, 16
	v_readlane_b32 s22, v28, 32
	v_readlane_b32 s23, v28, 48
	v_readlane_b32 s74, v30, 0
	v_readlane_b32 s25, v30, 16
	v_readlane_b32 s75, v30, 32
	v_readlane_b32 s76, v30, 48
	v_cmp_eq_u32_e32 vcc, s18, v6
	s_max_u32 s48, s48, s19
	s_max_u32 s22, s22, s23
	s_max_u32 s48, s48, s22
	s_max_u32 s74, s74, s25
	s_max_u32 s75, s75, s76
	s_max_u32 s74, s74, s75
	s_ff1_i32_b64 s76, vcc
	s_lshl_b64 s[100:101], 1, s76
	v_cndmask_b32_e64 v6, v6, v9, s[100:101]
	v_cndmask_b32_e64 v9, v9, v11, s[100:101]
	v_cndmask_b32_e64 v11, v11, v8, s[100:101]
	v_cndmask_b32_e64 v8, v8, 0, s[100:101]
	v_addc_co_u32_e64 v243, s[98:99], 0, v243, s[100:101]
	v_cmp_eq_u32_e32 vcc, s24, v12
	s_nop 0
	s_ff1_i32_b64 s76, vcc
	s_lshl_b64 s[100:101], 1, s76
	v_cndmask_b32_e64 v12, v12, v14, s[100:101]
	v_cndmask_b32_e64 v14, v14, v15, s[100:101]
	v_cndmask_b32_e64 v15, v15, v13, s[100:101]
	v_cndmask_b32_e64 v13, v13, 0, s[100:101]
	v_addc_co_u32_e64 v244, s[98:99], 0, v244, s[100:101]
	v_cmp_eq_u32_e32 vcc, s48, v16
	s_nop 0
	s_ff1_i32_b64 s76, vcc
	s_lshl_b64 s[100:101], 1, s76
	v_cndmask_b32_e64 v16, v16, v18, s[100:101]
	v_cndmask_b32_e64 v18, v18, v19, s[100:101]
	v_cndmask_b32_e64 v19, v19, v17, s[100:101]
	v_cndmask_b32_e64 v17, v17, 0, s[100:101]
	v_addc_co_u32_e64 v245, s[98:99], 0, v245, s[100:101]
	v_cmp_eq_u32_e32 vcc, s74, v20
	s_nop 0
	s_ff1_i32_b64 s76, vcc
	s_lshl_b64 s[100:101], 1, s76
	v_cndmask_b32_e64 v20, v20, v22, s[100:101]
	v_cndmask_b32_e64 v22, v22, v23, s[100:101]
	v_cndmask_b32_e64 v23, v23, v21, s[100:101]
	v_cndmask_b32_e64 v21, v21, 0, s[100:101]
	v_addc_co_u32_e64 v246, s[98:99], 0, v246, s[100:101]
	s_add_i32 s37, s37, -1
	s_cmp_eq_u32 s37, 0
	s_cbranch_scc0 .LBB0_1622
	v_lshlrev_b32_e32 v24, 2, v243
	v_bfe_u32 v24, v239, 0, v24
	v_lshrrev_b32_e32 v25, 8, v24
	v_or_b32_e32 v24, v24, v25
	v_lshrrev_b32_e32 v25, 4, v24
	v_or_b32_e32 v24, v24, v25
	v_and_b32_e32 v10, 15, v24
	v_lshlrev_b32_e32 v24, 2, v244
	v_bfe_u32 v24, v240, 0, v24
	v_lshrrev_b32_e32 v25, 8, v24
	v_or_b32_e32 v24, v24, v25
	v_lshrrev_b32_e32 v25, 4, v24
	v_or_b32_e32 v24, v24, v25
	v_and_b32_e32 v7, 15, v24
	v_lshlrev_b32_e32 v24, 2, v245
	v_bfe_u32 v24, v241, 0, v24
	v_lshrrev_b32_e32 v25, 8, v24
	v_or_b32_e32 v24, v24, v25
	v_lshrrev_b32_e32 v25, 4, v24
	v_or_b32_e32 v24, v24, v25
	v_and_b32_e32 v5, 15, v24
	v_lshlrev_b32_e32 v24, 2, v246
	v_bfe_u32 v24, v242, 0, v24
	v_lshrrev_b32_e32 v25, 8, v24
	v_or_b32_e32 v24, v24, v25
	v_lshrrev_b32_e32 v25, 4, v24
	v_or_b32_e32 v24, v24, v25
	v_and_b32_e32 v4, 15, v24
	s_lshl_b32 s18, 1, s36
	s_lshl_b32 s19, 2, s36
	v_bfe_i32 v6, v10, 0, 1
	v_bfe_i32 v8, v7, 0, 1
	v_and_b32_e32 v6, s18, v6
	v_and_b32_e32 v8, s19, v8
	v_or3_b32 v3, v6, v3, v8
	v_bfe_i32 v6, v10, 1, 1
	v_bfe_i32 v8, v7, 1, 1
	s_lshl_b32 s22, 4, s36
	s_lshl_b32 s23, 8, s36
	v_bfe_i32 v9, v5, 0, 1
	v_bfe_i32 v11, v4, 0, 1
	v_and_b32_e32 v6, s18, v6
	v_and_b32_e32 v8, s19, v8
	v_and_b32_e32 v9, s22, v9
	v_and_b32_e32 v11, s23, v11
	v_or3_b32 v2, v6, v2, v8
	v_bfe_i32 v6, v10, 2, 1
	v_bfe_i32 v8, v7, 2, 1
	v_or3_b32 v3, v3, v9, v11
	v_bfe_i32 v9, v5, 1, 1
	v_bfe_i32 v11, v4, 1, 1
	v_and_b32_e32 v6, s18, v6
	v_and_b32_e32 v8, s19, v8
	v_and_b32_e32 v9, s22, v9
	v_and_b32_e32 v11, s23, v11
	v_or3_b32 v1, v6, v1, v8
	v_bfe_i32 v6, v10, 3, 1
	v_bfe_i32 v7, v7, 3, 1
	v_or3_b32 v2, v2, v9, v11
	v_bfe_i32 v9, v5, 2, 1
	v_bfe_i32 v11, v4, 2, 1
	v_and_b32_e32 v6, s18, v6
	v_and_b32_e32 v7, s19, v7
	v_bfe_i32 v5, v5, 3, 1
	v_bfe_i32 v4, v4, 3, 1
	v_and_b32_e32 v9, s22, v9
	v_and_b32_e32 v11, s23, v11
	v_and_b32_e32 v5, s22, v5
	v_and_b32_e32 v4, s23, v4
	v_or3_b32 v0, v6, v0, v7
	v_or3_b32 v1, v1, v9, v11
	v_or3_b32 v0, v0, v5, v4
	s_mov_b64 s[18:19], 0
	s_and_b64 vcc, exec, s[60:61]
	s_cbranch_vccnz .LBB0_1625
	s_mov_b32 s36, 4
	s_branch .LBB0_1605
